# pipelined LDS phases: K3 msplit atomics batched, DPP wave scans in K1/K3, K1 scatter reads batched
# speedup vs baseline: 1.0234x; 1.0234x over previous
.LBB0_34:
	s_or_b64 exec, exec, s[26:27]
	v_and_b32_e32 v82, 3, v0
	v_and_b32_e32 v3, 0x3fc, v0
	v_lshl_or_b32 v3, v82, 12, v3
	v_add_u32_e32 v80, 0x12500, v3
	s_waitcnt lgkmcnt(0)
	s_barrier
	ds_read2st64_b32 v[18:19], v80 offset1:4
	v_add_u32_e32 v81, 0x16500, v3
	ds_read2st64_b32 v[20:21], v80 offset0:8 offset1:12
	ds_read2st64_b32 v[24:25], v81 offset1:4
	ds_read2st64_b32 v[22:23], v81 offset0:8 offset1:12
	s_waitcnt lgkmcnt(3)
	v_add_u32_e32 v3, v19, v18
	s_waitcnt lgkmcnt(1)
	v_add_u32_e32 v4, v25, v24
	v_add3_u32 v3, v3, v20, v21
	s_waitcnt lgkmcnt(0)
	v_add3_u32 v4, v4, v22, v23
	v_lshl_or_b32 v21, v4, 16, v3
	v_mov_b32_e32 v23, v21
	s_nop 1
	v_add_u32_dpp v23, v23, v23 row_shr:1 row_mask:0xf bank_mask:0xf
	s_nop 1
	v_add_u32_dpp v23, v23, v23 row_shr:2 row_mask:0xf bank_mask:0xf
	s_nop 1
	v_add_u32_dpp v23, v23, v23 row_shr:4 row_mask:0xf bank_mask:0xf
	s_nop 1
	v_add_u32_dpp v23, v23, v23 row_shr:8 row_mask:0xf bank_mask:0xf
	s_nop 1
	v_add_u32_dpp v23, v23, v23 row_bcast:15 row_mask:0xa bank_mask:0xf
	s_nop 1
	v_add_u32_dpp v23, v23, v23 row_bcast:31 row_mask:0xc bank_mask:0xf
	v_cmp_eq_u32_e64 s[26:27], 63, v2
	s_and_saveexec_b64 s[28:29], s[26:27]
	v_mov_b32_e32 v2, 0x1a500
	v_lshl_or_b32 v2, v53, 2, v2
	ds_write_b32 v2, v23
	s_or_b64 exec, exec, s[28:29]
	v_mov_b32_e32 v2, 0x1a500
	s_waitcnt lgkmcnt(0)
	s_barrier
	ds_read_b128 v[2:5], v2
	v_mov_b32_e32 v6, 0x1a510
	ds_read_b128 v[6:9], v6
	v_cmp_lt_u32_e64 s[26:27], 63, v0
	s_movk_i32 s3, 0x7f
	v_mov_b32_e32 v10, 0x1a520
	s_waitcnt lgkmcnt(1)
	v_cndmask_b32_e64 v83, 0, v2, s[26:27]
	v_cmp_lt_u32_e64 s[26:27], s3, v0
	s_movk_i32 s3, 0xbf
	ds_read_b128 v[10:13], v10
	v_cndmask_b32_e64 v84, 0, v3, s[26:27]
	v_cmp_lt_u32_e64 s[26:27], s3, v0
	s_movk_i32 s3, 0xff
	v_mov_b32_e32 v14, 0x1a530
	v_cndmask_b32_e64 v85, 0, v4, s[26:27]
	v_cmp_lt_u32_e64 s[26:27], s3, v0
	s_movk_i32 s3, 0x13f
	ds_read_b128 v[14:17], v14
	v_cndmask_b32_e64 v86, 0, v5, s[26:27]
	v_cmp_lt_u32_e64 s[26:27], s3, v0
	s_movk_i32 s3, 0x17f
	v_sub_u32_e32 v21, v23, v21
	s_waitcnt lgkmcnt(2)
	v_cndmask_b32_e64 v87, 0, v6, s[26:27]
	v_cmp_lt_u32_e64 s[26:27], s3, v0
	s_movk_i32 s3, 0x1bf
	v_add_u32_e32 v21, v83, v21
	v_cndmask_b32_e64 v88, 0, v7, s[26:27]
	v_cmp_lt_u32_e64 s[26:27], s3, v0
	s_movk_i32 s3, 0x1ff
	v_add3_u32 v21, v21, v84, v85
	v_cndmask_b32_e64 v89, 0, v8, s[26:27]
	v_cmp_lt_u32_e64 s[26:27], s3, v0
	s_movk_i32 s3, 0x23f
	v_add3_u32 v21, v21, v86, v87
	v_cndmask_b32_e64 v90, 0, v9, s[26:27]
	v_cmp_lt_u32_e64 s[26:27], s3, v0
	s_movk_i32 s3, 0x27f
	v_add3_u32 v21, v21, v88, v89
	s_waitcnt lgkmcnt(1)
	v_cndmask_b32_e64 v91, 0, v10, s[26:27]
	v_cmp_lt_u32_e64 s[26:27], s3, v0
	s_movk_i32 s3, 0x2bf
	v_add3_u32 v21, v21, v90, v91
	v_cndmask_b32_e64 v92, 0, v11, s[26:27]
	v_cmp_lt_u32_e64 s[26:27], s3, v0
	s_movk_i32 s3, 0x2ff
	s_mul_i32 s28, s2, 0x101
	v_cndmask_b32_e64 v93, 0, v12, s[26:27]
	v_cmp_lt_u32_e64 s[26:27], s3, v0
	s_movk_i32 s3, 0x33f
	v_add3_u32 v21, v21, v92, v93
	v_cndmask_b32_e64 v94, 0, v13, s[26:27]
	v_cmp_lt_u32_e64 s[26:27], s3, v0
	s_movk_i32 s3, 0x37f
	s_waitcnt lgkmcnt(0)
	v_cndmask_b32_e64 v95, 0, v14, s[26:27]
	v_cmp_lt_u32_e64 s[26:27], s3, v0
	v_add3_u32 v21, v21, v94, v95
	s_nop 0
	v_cndmask_b32_e64 v96, 0, v15, s[26:27]
	v_cmp_eq_u32_e64 s[26:27], 15, v53
	s_nop 1
	v_cndmask_b32_e64 v53, 0, v16, s[26:27]
	v_add3_u32 v21, v21, v96, v53
	v_and_b32_e32 v23, 0xffff, v21
	v_lshrrev_b32_e32 v21, 16, v21
	v_cmp_eq_u32_e64 s[26:27], 0, v82
	s_and_saveexec_b64 s[30:31], s[26:27]
	s_cbranch_execz .LBB0_38
	v_lshrrev_b32_e32 v53, 2, v0
	v_add_u32_e32 v82, s28, v53
	v_ashrrev_i32_e32 v83, 31, v82
	v_lshlrev_b64 v[82:83], 2, v[82:83]
	v_lshl_add_u64 v[84:85], s[40:41], 0, v[82:83]
	v_lshl_add_u64 v[82:83], s[42:43], 0, v[82:83]
	global_store_dword v[84:85], v23, off
	global_store_dword v[82:83], v21, off

.LBB0_40:
	s_or_b64 exec, exec, s[30:31]
	v_add_u32_e32 v2, v18, v23
	v_add_u32_e32 v3, v24, v21
	ds_write2st64_b32 v80, v23, v2 offset1:4
	v_add_u32_e32 v2, v19, v2
	ds_write2st64_b32 v81, v21, v3 offset1:4
	v_add_u32_e32 v3, v25, v3
	v_add_u32_e32 v4, v20, v2
	v_add_u32_e32 v5, v22, v3
	ds_write2st64_b32 v80, v2, v4 offset0:8 offset1:12
	ds_write2st64_b32 v81, v3, v5 offset0:8 offset1:12
	s_waitcnt lgkmcnt(0)
	s_barrier
	s_mov_b64 s[44:45], exec
	s_mov_b32 s46, 0x51eb851f
	s_movk_i32 s47, 0x7e70
	s_mov_b32 s48, 0xfe70
	s_waitcnt vmcnt(4)
	s_and_b64 exec, s[44:45], s[22:23]
	v_mul_hi_u32 v2, v51, s46
	v_mul_hi_u32 v4, v52, s46
	v_lshrrev_b32_e32 v2, 7, v2
	v_lshrrev_b32_e32 v4, 7, v4
	v_lshl_add_u32 v3, v2, 2, v29
	v_lshl_add_u32 v5, v4, 2, v27
	ds_read_b32 v97, v3
	ds_read_b32 v98, v5
	v_mad_u32_u24 v4, v4, s47, v52
	v_lshl_or_b32 v52, v4, 17, v51
	v_mad_u32_u24 v51, v2, s48, v51
	s_and_b64 exec, s[44:45], s[20:21]
	v_mul_hi_u32 v2, v49, s46
	v_mul_hi_u32 v4, v50, s46
	v_lshrrev_b32_e32 v2, 7, v2
	v_lshrrev_b32_e32 v4, 7, v4
	v_lshl_add_u32 v3, v2, 2, v29
	v_lshl_add_u32 v5, v4, 2, v27
	ds_read_b32 v99, v3
	ds_read_b32 v100, v5
	v_mad_u32_u24 v4, v4, s47, v50
	v_lshl_or_b32 v50, v4, 17, v49
	v_mad_u32_u24 v49, v2, s48, v49
	s_and_b64 exec, s[44:45], s[18:19]
	v_mul_hi_u32 v2, v47, s46
	v_mul_hi_u32 v4, v48, s46
	v_lshrrev_b32_e32 v2, 7, v2
	v_lshrrev_b32_e32 v4, 7, v4
	v_lshl_add_u32 v3, v2, 2, v29
	v_lshl_add_u32 v5, v4, 2, v27
	ds_read_b32 v101, v3
	ds_read_b32 v102, v5
	v_mad_u32_u24 v4, v4, s47, v48
	v_lshl_or_b32 v48, v4, 17, v47
	v_mad_u32_u24 v47, v2, s48, v47
	s_and_b64 exec, s[44:45], s[16:17]
	v_mul_hi_u32 v2, v45, s46
	v_mul_hi_u32 v4, v46, s46
	v_lshrrev_b32_e32 v2, 7, v2
	v_lshrrev_b32_e32 v4, 7, v4
	v_lshl_add_u32 v3, v2, 2, v29
	v_lshl_add_u32 v5, v4, 2, v27
	ds_read_b32 v103, v3
	ds_read_b32 v104, v5
	v_mad_u32_u24 v4, v4, s47, v46
	v_lshl_or_b32 v46, v4, 17, v45
	v_mad_u32_u24 v45, v2, s48, v45
	s_and_b64 exec, s[44:45], s[14:15]
	v_mul_hi_u32 v2, v43, s46
	v_mul_hi_u32 v4, v44, s46
	v_lshrrev_b32_e32 v2, 7, v2
	v_lshrrev_b32_e32 v4, 7, v4
	v_lshl_add_u32 v3, v2, 2, v29
	v_lshl_add_u32 v5, v4, 2, v27
	ds_read_b32 v105, v3
	ds_read_b32 v106, v5
	v_mad_u32_u24 v4, v4, s47, v44
	v_lshl_or_b32 v44, v4, 17, v43
	v_mad_u32_u24 v43, v2, s48, v43
	s_and_b64 exec, s[44:45], s[12:13]
	v_mul_hi_u32 v2, v41, s46
	v_mul_hi_u32 v4, v42, s46
	v_lshrrev_b32_e32 v2, 7, v2
	v_lshrrev_b32_e32 v4, 7, v4
	v_lshl_add_u32 v3, v2, 2, v29
	v_lshl_add_u32 v5, v4, 2, v27
	ds_read_b32 v107, v3
	ds_read_b32 v108, v5
	v_mad_u32_u24 v4, v4, s47, v42
	v_lshl_or_b32 v42, v4, 17, v41
	v_mad_u32_u24 v41, v2, s48, v41
	s_and_b64 exec, s[44:45], s[10:11]
	v_mul_hi_u32 v2, v39, s46
	v_mul_hi_u32 v4, v40, s46
	v_lshrrev_b32_e32 v2, 7, v2
	v_lshrrev_b32_e32 v4, 7, v4
	v_lshl_add_u32 v3, v2, 2, v29
	v_lshl_add_u32 v5, v4, 2, v27
	ds_read_b32 v109, v3
	ds_read_b32 v110, v5
	v_mad_u32_u24 v4, v4, s47, v40
	v_lshl_or_b32 v40, v4, 17, v39
	v_mad_u32_u24 v39, v2, s48, v39
	s_and_b64 exec, s[44:45], s[22:23]
	s_waitcnt lgkmcnt(12)
	v_add_u32_e32 v5, v98, v78
	v_lshlrev_b32_e32 v5, 2, v5
	ds_write_b32 v5, v52
	v_add_u32_e32 v3, v97, v79
	v_lshlrev_b32_e32 v3, 1, v3
	ds_write_b16 v3, v51 offset:50000
	s_and_b64 exec, s[44:45], s[20:21]
	s_waitcnt lgkmcnt(12)
	v_add_u32_e32 v5, v100, v77
	v_lshlrev_b32_e32 v5, 2, v5
	ds_write_b32 v5, v50
	v_add_u32_e32 v3, v99, v60
	v_lshlrev_b32_e32 v3, 1, v3
	ds_write_b16 v3, v49 offset:50000
	s_and_b64 exec, s[44:45], s[18:19]
	s_waitcnt lgkmcnt(12)
	v_add_u32_e32 v5, v102, v76
	v_lshlrev_b32_e32 v5, 2, v5
	ds_write_b32 v5, v48
	v_add_u32_e32 v3, v101, v75
	v_lshlrev_b32_e32 v3, 1, v3
	ds_write_b16 v3, v47 offset:50000
	s_and_b64 exec, s[44:45], s[16:17]
	s_waitcnt lgkmcnt(12)
	v_add_u32_e32 v5, v104, v74
	v_lshlrev_b32_e32 v5, 2, v5
	ds_write_b32 v5, v46
	v_add_u32_e32 v3, v103, v58
	v_lshlrev_b32_e32 v3, 1, v3
	ds_write_b16 v3, v45 offset:50000
	s_and_b64 exec, s[44:45], s[14:15]
	s_waitcnt lgkmcnt(12)
	v_add_u32_e32 v5, v106, v73
	v_lshlrev_b32_e32 v5, 2, v5
	ds_write_b32 v5, v44
	v_add_u32_e32 v3, v105, v72
	v_lshlrev_b32_e32 v3, 1, v3
	ds_write_b16 v3, v43 offset:50000
	s_and_b64 exec, s[44:45], s[12:13]
	s_waitcnt lgkmcnt(12)
	v_add_u32_e32 v5, v108, v71
	v_lshlrev_b32_e32 v5, 2, v5
	ds_write_b32 v5, v42
	v_add_u32_e32 v3, v107, v57
	v_lshlrev_b32_e32 v3, 1, v3
	ds_write_b16 v3, v41 offset:50000
	s_and_b64 exec, s[44:45], s[10:11]
	s_waitcnt lgkmcnt(12)
	v_add_u32_e32 v5, v110, v70
	v_lshlrev_b32_e32 v5, 2, v5
	ds_write_b32 v5, v40
	v_add_u32_e32 v3, v109, v69
	v_lshlrev_b32_e32 v3, 1, v3
	ds_write_b16 v3, v39 offset:50000
	s_waitcnt lgkmcnt(2)
	s_and_b64 exec, s[44:45], s[8:9]
	v_mul_hi_u32 v2, v37, s46
	v_mul_hi_u32 v4, v38, s46
	v_lshrrev_b32_e32 v2, 7, v2
	v_lshrrev_b32_e32 v4, 7, v4
	v_lshl_add_u32 v3, v2, 2, v29
	v_lshl_add_u32 v5, v4, 2, v27
	ds_read_b32 v111, v3
	ds_read_b32 v112, v5
	v_mad_u32_u24 v4, v4, s47, v38
	v_lshl_or_b32 v38, v4, 17, v37
	v_mad_u32_u24 v37, v2, s48, v37
	s_and_b64 exec, s[44:45], s[6:7]
	v_mul_hi_u32 v2, v35, s46
	v_mul_hi_u32 v4, v36, s46
	v_lshrrev_b32_e32 v2, 7, v2
	v_lshrrev_b32_e32 v4, 7, v4
	v_lshl_add_u32 v3, v2, 2, v29
	v_lshl_add_u32 v5, v4, 2, v27
	ds_read_b32 v113, v3
	ds_read_b32 v114, v5
	v_mad_u32_u24 v4, v4, s47, v36
	v_lshl_or_b32 v36, v4, 17, v35
	v_mad_u32_u24 v35, v2, s48, v35
	s_and_b64 exec, s[44:45], s[4:5]
	v_mul_hi_u32 v2, v33, s46
	v_mul_hi_u32 v4, v34, s46
	v_lshrrev_b32_e32 v2, 7, v2
	v_lshrrev_b32_e32 v4, 7, v4
	v_lshl_add_u32 v3, v2, 2, v29
	v_lshl_add_u32 v5, v4, 2, v27
	ds_read_b32 v115, v3
	ds_read_b32 v116, v5
	v_mad_u32_u24 v4, v4, s47, v34
	v_lshl_or_b32 v34, v4, 17, v33
	v_mad_u32_u24 v33, v2, s48, v33
	s_and_b64 exec, s[44:45], s[24:25]
	v_mul_hi_u32 v2, v31, s46
	v_mul_hi_u32 v4, v32, s46
	v_lshrrev_b32_e32 v2, 7, v2
	v_lshrrev_b32_e32 v4, 7, v4
	v_lshl_add_u32 v3, v2, 2, v29
	v_lshl_add_u32 v5, v4, 2, v27
	ds_read_b32 v117, v3
	ds_read_b32 v118, v5
	v_mad_u32_u24 v4, v4, s47, v32
	v_lshl_or_b32 v32, v4, 17, v31
	v_mad_u32_u24 v31, v2, s48, v31
	s_and_b64 exec, s[44:45], s[0:1]
	v_mul_hi_u32 v2, v28, s46
	v_mul_hi_u32 v4, v30, s46
	v_lshrrev_b32_e32 v2, 7, v2
	v_lshrrev_b32_e32 v4, 7, v4
	v_lshl_add_u32 v3, v2, 2, v29
	v_lshl_add_u32 v5, v4, 2, v27
	ds_read_b32 v119, v3
	ds_read_b32 v120, v5
	v_mad_u32_u24 v4, v4, s47, v30
	v_lshl_or_b32 v30, v4, 17, v28
	v_mad_u32_u24 v28, v2, s48, v28
	s_and_b64 exec, s[44:45], vcc
	v_mul_hi_u32 v2, v1, s46
	v_mul_hi_u32 v4, v26, s46
	v_lshrrev_b32_e32 v2, 7, v2
	v_lshrrev_b32_e32 v4, 7, v4
	v_lshl_add_u32 v3, v2, 2, v29
	v_lshl_add_u32 v5, v4, 2, v27
	ds_read_b32 v121, v3
	ds_read_b32 v122, v5
	v_mad_u32_u24 v4, v4, s47, v26
	v_lshl_or_b32 v26, v4, 17, v1
	v_mad_u32_u24 v1, v2, s48, v1
	s_and_b64 exec, s[44:45], s[8:9]
	s_waitcnt lgkmcnt(10)
	v_add_u32_e32 v5, v112, v68
	v_lshlrev_b32_e32 v5, 2, v5
	ds_write_b32 v5, v38
	v_add_u32_e32 v3, v111, v56
	v_lshlrev_b32_e32 v3, 1, v3
	ds_write_b16 v3, v37 offset:50000
	s_and_b64 exec, s[44:45], s[6:7]
	s_waitcnt lgkmcnt(10)
	v_add_u32_e32 v5, v114, v67
	v_lshlrev_b32_e32 v5, 2, v5
	ds_write_b32 v5, v36
	v_add_u32_e32 v3, v113, v66
	v_lshlrev_b32_e32 v3, 1, v3
	ds_write_b16 v3, v35 offset:50000
	s_and_b64 exec, s[44:45], s[4:5]
	s_waitcnt lgkmcnt(10)
	v_add_u32_e32 v5, v116, v65
	v_lshlrev_b32_e32 v5, 2, v5
	ds_write_b32 v5, v34
	v_add_u32_e32 v3, v115, v55
	v_lshlrev_b32_e32 v3, 1, v3
	ds_write_b16 v3, v33 offset:50000
	s_and_b64 exec, s[44:45], s[24:25]
	s_waitcnt lgkmcnt(10)
	v_add_u32_e32 v5, v118, v64
	v_lshlrev_b32_e32 v5, 2, v5
	ds_write_b32 v5, v32
	v_add_u32_e32 v3, v117, v63
	v_lshlrev_b32_e32 v3, 1, v3
	ds_write_b16 v3, v31 offset:50000
	s_and_b64 exec, s[44:45], s[0:1]
	s_waitcnt lgkmcnt(10)
	v_add_u32_e32 v5, v120, v62
	v_lshlrev_b32_e32 v5, 2, v5
	ds_write_b32 v5, v30
	v_add_u32_e32 v3, v119, v54
	v_lshlrev_b32_e32 v3, 1, v3
	ds_write_b16 v3, v28 offset:50000
	s_and_b64 exec, s[44:45], vcc
	s_waitcnt lgkmcnt(10)
	v_add_u32_e32 v5, v122, v61
	v_lshlrev_b32_e32 v5, 2, v5
	ds_write_b32 v5, v26
	v_add_u32_e32 v3, v121, v59
	v_lshlrev_b32_e32 v3, 1, v3
	ds_write_b16 v3, v1 offset:50000
.LBB0_54:
	s_mov_b64 exec, s[44:45]
	s_waitcnt vmcnt(1)
	v_lshlrev_b32_e32 v1, 4, v0
	v_lshlrev_b32_e32 v20, 3, v0
	s_waitcnt lgkmcnt(0)
	s_barrier
	s_mul_hi_i32 s35, s2, 0x30d4
	v_add_u32_e32 v2, 0x150, v20
	ds_read_b128 v[6:9], v1
	s_lshl_b64 s[0:1], s[34:35], 2
	v_add_u32_e32 v10, 0xc350, v20
	ds_read2st64_b64 v[2:5], v2 offset0:97 offset1:113
	s_add_u32 s0, s36, s0
	v_or_b32_e32 v21, 0x400, v0
	v_or_b32_e32 v22, 0x800, v0
	v_or_b32_e32 v0, 0xc00, v0
	s_movk_i32 s2, 0xc35
	ds_read_b64 v[18:19], v10 offset:16384
	ds_read_b128 v[10:13], v1 offset:16384
	ds_read_b128 v[14:17], v1 offset:32768
	s_addc_u32 s1, s37, s1
	v_cmp_gt_u32_e32 vcc, s2, v0
	s_lshl_b64 s[2:3], s[34:35], 1
	s_add_u32 s2, s38, s2
	s_addc_u32 s3, s39, s3
	s_waitcnt lgkmcnt(4)
	global_store_dwordx4 v1, v[6:9], s[0:1]
	s_waitcnt lgkmcnt(3)
	global_store_dwordx2 v20, v[2:3], s[2:3]
	v_lshlrev_b32_e32 v2, 4, v21
	v_lshlrev_b32_e32 v1, 3, v21
	s_waitcnt lgkmcnt(1)
	global_store_dwordx4 v2, v[10:13], s[0:1]
	global_store_dwordx2 v1, v[4:5], s[2:3]
	v_lshlrev_b32_e32 v2, 4, v22
	v_lshlrev_b32_e32 v1, 3, v22
	s_waitcnt lgkmcnt(0)
	global_store_dwordx4 v2, v[14:17], s[0:1]
	global_store_dwordx2 v1, v[18:19], s[2:3]
	s_and_saveexec_b64 s[4:5], vcc
	s_cbranch_execz .LBB0_56
	v_cndmask_b32_e32 v1, 0, v0, vcc
	v_lshlrev_b32_e32 v6, 3, v1
	v_lshlrev_b32_e32 v1, 4, v1
	ds_read_b128 v[2:5], v1
	ds_read_b64 v[6:7], v6 offset:50000
	v_lshlrev_b32_e32 v1, 3, v0
	v_lshlrev_b32_e32 v0, 4, v0
	s_waitcnt lgkmcnt(1)
	global_store_dwordx4 v0, v[2:5], s[0:1]
	s_waitcnt lgkmcnt(0)
	global_store_dwordx2 v1, v[6:7], s[2:3]

	.amdhsa_kernel _Z6k_partPKiS0_PjPtS1_S1_S1_
		.amdhsa_group_segment_fixed_size 107840
		.amdhsa_private_segment_fixed_size 0
		.amdhsa_kernarg_size 56
		.amdhsa_user_sgpr_count 2
		.amdhsa_user_sgpr_dispatch_ptr 0
		.amdhsa_user_sgpr_queue_ptr 0
		.amdhsa_user_sgpr_kernarg_segment_ptr 1
		.amdhsa_user_sgpr_dispatch_id 0
		.amdhsa_user_sgpr_kernarg_preload_length 0
		.amdhsa_user_sgpr_kernarg_preload_offset 0
		.amdhsa_user_sgpr_private_segment_size 0
		.amdhsa_uses_dynamic_stack 0
		.amdhsa_enable_private_segment 0
		.amdhsa_system_sgpr_workgroup_id_x 1
		.amdhsa_system_sgpr_workgroup_id_y 0
		.amdhsa_system_sgpr_workgroup_id_z 0
		.amdhsa_system_sgpr_workgroup_info 0
		.amdhsa_system_vgpr_workitem_id 0
		.amdhsa_next_free_vgpr 123
		.amdhsa_next_free_sgpr 96
		.amdhsa_accum_offset 124
		.amdhsa_reserve_vcc 1
		.amdhsa_float_round_mode_32 0
		.amdhsa_float_round_mode_16_64 0
		.amdhsa_float_denorm_mode_32 3
		.amdhsa_float_denorm_mode_16_64 3
		.amdhsa_dx10_clamp 1
		.amdhsa_ieee_mode 1
		.amdhsa_fp16_overflow 0
		.amdhsa_tg_split 0
		.amdhsa_exception_fp_ieee_invalid_op 0
		.amdhsa_exception_fp_denorm_src 0
		.amdhsa_exception_fp_ieee_div_zero 0
		.amdhsa_exception_fp_ieee_overflow 0
		.amdhsa_exception_fp_ieee_underflow 0
		.amdhsa_exception_fp_ieee_inexact 0
		.amdhsa_exception_int_div_zero 0
	.end_amdhsa_kernel

.LBB2_99:
	s_movk_i32 s2, 0x190
	v_mov_b32_e32 v2, 0x10000
	v_cmp_gt_u32_e32 vcc, s2, v0
	v_lshl_or_b32 v35, v0, 2, v2
	v_mov_b32_e32 v36, 0
	v_mov_b32_e32 v37, 0
	s_waitcnt lgkmcnt(0)
	s_barrier
	s_lshl_b32 s84, s83, 10
	v_add_u32_e32 v112, s84, v0
	v_min_u32_e32 v112, 0x61a7, v112
	v_lshlrev_b32_e32 v112, 7, v112
	global_load_dword v112, v112, s[56:57]
	s_and_saveexec_b64 s[2:3], vcc
	ds_read_b32 v37, v35
	s_or_b64 exec, exec, s[2:3]
	s_and_saveexec_b64 s[2:3], vcc
	ds_read_b32 v36, v35 offset:1600
	s_or_b64 exec, exec, s[2:3]
	v_mov_b32_e32 v38, 0
	v_mov_b32_e32 v39, 0
	s_and_saveexec_b64 s[2:3], vcc
	ds_read_b32 v39, v35 offset:3200
	s_or_b64 exec, exec, s[2:3]
	s_and_saveexec_b64 s[2:3], vcc
	ds_read_b32 v38, v35 offset:4800
	s_or_b64 exec, exec, s[2:3]
	v_mov_b32_e32 v40, 0
	v_mov_b32_e32 v41, 0
	s_and_saveexec_b64 s[2:3], vcc
	ds_read_b32 v41, v35 offset:6400
	s_or_b64 exec, exec, s[2:3]
	s_and_saveexec_b64 s[2:3], vcc
	ds_read_b32 v40, v35 offset:8000
	s_or_b64 exec, exec, s[2:3]
	v_mov_b32_e32 v43, 0
	v_mov_b32_e32 v44, 0
	s_and_saveexec_b64 s[2:3], vcc
	ds_read_b32 v44, v35 offset:9600
	s_or_b64 exec, exec, s[2:3]
	s_and_saveexec_b64 s[2:3], vcc
	ds_read_b32 v43, v35 offset:11200
	s_or_b64 exec, exec, s[2:3]
	v_mov_b32_e32 v46, 0
	v_mov_b32_e32 v47, 0
	s_and_saveexec_b64 s[2:3], vcc
	ds_read_b32 v47, v35 offset:12800
	s_or_b64 exec, exec, s[2:3]
	s_and_saveexec_b64 s[2:3], vcc
	ds_read_b32 v46, v35 offset:14400
	s_or_b64 exec, exec, s[2:3]
	v_mov_b32_e32 v53, 0
	v_mov_b32_e32 v54, 0
	s_and_saveexec_b64 s[2:3], vcc
	ds_read_b32 v54, v35 offset:16000
	s_or_b64 exec, exec, s[2:3]
	s_and_saveexec_b64 s[2:3], vcc
	ds_read_b32 v53, v35 offset:17600
	s_or_b64 exec, exec, s[2:3]
	v_mov_b32_e32 v55, 0
	v_mov_b32_e32 v56, 0
	s_and_saveexec_b64 s[2:3], vcc
	ds_read_b32 v56, v35 offset:19200
	s_or_b64 exec, exec, s[2:3]
	s_and_saveexec_b64 s[2:3], vcc
	ds_read_b32 v55, v35 offset:20800
	s_or_b64 exec, exec, s[2:3]
	v_mov_b32_e32 v2, 0
	v_mov_b32_e32 v57, 0
	s_and_saveexec_b64 s[2:3], vcc
	ds_read_b32 v57, v35 offset:22400
	s_or_b64 exec, exec, s[2:3]
	s_and_saveexec_b64 s[2:3], vcc
	ds_read_b32 v2, v35 offset:24000
	s_or_b64 exec, exec, s[2:3]
	s_waitcnt lgkmcnt(0)
	v_add_u32_e32 v3, v36, v37
	v_add3_u32 v3, v39, v3, v38
	v_add3_u32 v3, v41, v3, v40
	v_add3_u32 v3, v44, v3, v43
	v_add3_u32 v3, v47, v3, v46
	v_add3_u32 v3, v54, v3, v53
	v_add3_u32 v3, v56, v3, v55
	v_add3_u32 v58, v57, v3, v2
	v_mbcnt_lo_u32_b32 v2, -1, 0
	v_mbcnt_hi_u32_b32 v51, -1, v2
	v_and_b32_e32 v52, 64, v51
	v_mov_b32_e32 v59, v58
	s_nop 1
	v_add_u32_dpp v59, v59, v59 row_shr:1 row_mask:0xf bank_mask:0xf
	s_nop 1
	v_add_u32_dpp v59, v59, v59 row_shr:2 row_mask:0xf bank_mask:0xf
	s_nop 1
	v_add_u32_dpp v59, v59, v59 row_shr:4 row_mask:0xf bank_mask:0xf
	s_nop 1
	v_add_u32_dpp v59, v59, v59 row_shr:8 row_mask:0xf bank_mask:0xf
	s_nop 1
	v_add_u32_dpp v59, v59, v59 row_bcast:15 row_mask:0xa bank_mask:0xf
	s_nop 1
	v_add_u32_dpp v59, v59, v59 row_bcast:31 row_mask:0xc bank_mask:0xf
	v_cmp_eq_u32_e64 s[2:3], 63, v45
	s_and_saveexec_b64 s[4:5], s[2:3]
	s_xor_b64 s[2:3], exec, s[4:5]
	v_mov_b32_e32 v2, 0x17cf0
	v_lshl_add_u32 v2, v6, 2, v2
	ds_write_b32 v2, v59
	s_or_b64 exec, exec, s[2:3]
	v_mov_b32_e32 v2, 0x17cf0
	v_mov_b32_e32 v3, 0x17d00
	s_waitcnt lgkmcnt(0)
	s_barrier
	ds_read_b128 v[14:17], v2
	ds_read_b128 v[6:9], v3
	v_mov_b32_e32 v2, 0x17d10
	v_mov_b32_e32 v3, 0x17d20
	ds_read_b128 v[10:13], v2
	ds_read_b128 v[2:5], v3
	s_and_saveexec_b64 s[2:3], vcc
	s_cbranch_execz .LBB2_135
	v_cmp_lt_u32_e32 vcc, 63, v0
	s_movk_i32 s4, 0x7f
	v_sub_u32_e32 v58, v59, v58
	s_waitcnt lgkmcnt(3)
	v_cndmask_b32_e32 v60, 0, v14, vcc
	v_cmp_lt_u32_e32 vcc, s4, v0
	s_movk_i32 s4, 0xbf
	s_nop 0
	v_cndmask_b32_e32 v59, 0, v15, vcc
	v_cmp_lt_u32_e32 vcc, s4, v0
	s_movk_i32 s4, 0xff
	v_add3_u32 v58, v60, v58, v59
	v_cndmask_b32_e32 v59, 0, v16, vcc
	v_cmp_lt_u32_e32 vcc, s4, v0
	s_movk_i32 s4, 0x13f
	s_nop 0
	v_cndmask_b32_e32 v60, 0, v17, vcc
	v_cmp_lt_u32_e32 vcc, s4, v0
	s_movk_i32 s4, 0x17f
	v_add3_u32 v58, v58, v59, v60
	s_waitcnt lgkmcnt(2)
	v_cndmask_b32_e32 v59, 0, v6, vcc
	v_cmp_lt_u32_e32 vcc, s4, v0
	s_nop 1
	v_cndmask_b32_e32 v60, 0, v7, vcc
	v_add3_u32 v58, v58, v59, v60
	v_add_u32_e32 v37, v37, v58
	v_add_u32_e32 v36, v36, v37
	ds_write_b32 v35, v36 offset:3200
	v_add_u32_e32 v36, v39, v36
	ds_write_b32 v35, v36 offset:4800
	v_add_u32_e32 v36, v38, v36
	ds_write_b32 v35, v36 offset:6400
	v_add_u32_e32 v36, v41, v36
	ds_write_b32 v35, v36 offset:8000
	v_add_u32_e32 v36, v40, v36
	ds_write_b32 v35, v36 offset:9600
	v_add_u32_e32 v36, v44, v36
	ds_write_b32 v35, v36 offset:11200
	v_add_u32_e32 v36, v43, v36
	ds_write_b32 v35, v36 offset:12800
	v_add_u32_e32 v36, v47, v36
	ds_write_b32 v35, v36 offset:14400
	v_add_u32_e32 v36, v46, v36
	ds_write_b32 v35, v36 offset:16000
	v_add_u32_e32 v36, v54, v36
	ds_write_b32 v35, v36 offset:17600
	v_add_u32_e32 v36, v53, v36
	ds_write_b32 v35, v36 offset:19200
	v_add_u32_e32 v36, v56, v36
	ds_write_b32 v35, v36 offset:20800
	v_add_u32_e32 v36, v55, v36
	ds_write_b32 v35, v36 offset:22400
	v_add_u32_e32 v36, v57, v36
	ds_write_b32 v35, v58
	ds_write_b32 v35, v37 offset:1600
	ds_write_b32 v35, v36 offset:24000
	v_mov_b32_e32 v35, 0x16e00
	v_lshl_add_u32 v35, v0, 2, v35
	ds_write_b32 v35, v58
.LBB2_135:
	s_or_b64 exec, exec, s[2:3]
	s_waitcnt lgkmcnt(3)
	v_add_u32_e32 v14, v15, v14
	v_add_u32_e32 v14, v14, v16
	v_add_u32_e32 v14, v14, v17
	s_waitcnt lgkmcnt(2)
	v_add_u32_e32 v6, v14, v6
	v_add_u32_e32 v6, v6, v7
	v_add_u32_e32 v6, v6, v8
	v_add_u32_e32 v6, v6, v9
	s_waitcnt lgkmcnt(1)
	v_add_u32_e32 v6, v6, v10
	v_add_u32_e32 v6, v6, v11
	v_add_u32_e32 v6, v6, v12
	v_add_u32_e32 v6, v6, v13
	s_waitcnt lgkmcnt(0)
	v_add_u32_e32 v2, v6, v2
	v_add_u32_e32 v2, v2, v3
	v_add_u32_e32 v2, v2, v4
	v_add_u32_e32 v2, v2, v5
	s_and_saveexec_b64 s[2:3], s[44:45]
	v_mov_b32_e32 v3, 0x17440
	ds_write_b32 v3, v2
	s_or_b64 exec, exec, s[2:3]
	s_movk_i32 s2, 0x4000
	v_cmp_lt_u32_e64 s[6:7], s2, v2
	s_movk_i32 s2, 0x4001
	v_cmp_gt_u32_e64 s[4:5], s2, v2
	s_mov_b64 s[2:3], -1
	s_and_b64 vcc, exec, s[4:5]
	s_waitcnt lgkmcnt(0)
	s_barrier
	s_cbranch_vccz .LBB2_252
	v_mov_b32_e32 v3, 1
	s_mov_b64 s[2:3], exec
	s_and_b64 exec, s[2:3], s[20:21]
	v_lshrrev_b32_e32 v82, 15, v19
	v_and_b32_e32 v82, 0x1fffc, v82
	v_add_u32_e32 v82, v18, v82
	ds_add_rtn_u32 v66, v82, v3
	s_and_b64 exec, s[2:3], s[8:9]
	v_lshrrev_b32_e32 v82, 15, v20
	v_and_b32_e32 v82, 0x1fffc, v82
	v_add_u32_e32 v82, v18, v82
	ds_add_rtn_u32 v67, v82, v3
	s_and_b64 exec, s[2:3], s[10:11]
	v_lshrrev_b32_e32 v82, 15, v21
	v_and_b32_e32 v82, 0x1fffc, v82
	v_add_u32_e32 v82, v18, v82
	ds_add_rtn_u32 v68, v82, v3
	s_and_b64 exec, s[2:3], s[12:13]
	v_lshrrev_b32_e32 v82, 15, v22
	v_and_b32_e32 v82, 0x1fffc, v82
	v_add_u32_e32 v82, v18, v82
	ds_add_rtn_u32 v69, v82, v3
	s_and_b64 exec, s[2:3], s[14:15]
	v_lshrrev_b32_e32 v82, 15, v23
	v_and_b32_e32 v82, 0x1fffc, v82
	v_add_u32_e32 v82, v18, v82
	ds_add_rtn_u32 v70, v82, v3
	s_and_b64 exec, s[2:3], s[16:17]
	v_lshrrev_b32_e32 v82, 15, v24
	v_and_b32_e32 v82, 0x1fffc, v82
	v_add_u32_e32 v82, v18, v82
	ds_add_rtn_u32 v71, v82, v3
	s_and_b64 exec, s[2:3], s[18:19]
	v_lshrrev_b32_e32 v82, 15, v25
	v_and_b32_e32 v82, 0x1fffc, v82
	v_add_u32_e32 v82, v18, v82
	ds_add_rtn_u32 v72, v82, v3
	s_and_b64 exec, s[2:3], s[22:23]
	v_lshrrev_b32_e32 v82, 15, v26
	v_and_b32_e32 v82, 0x1fffc, v82
	v_add_u32_e32 v82, v18, v82
	ds_add_rtn_u32 v73, v82, v3
	s_and_b64 exec, s[2:3], s[20:21]
	s_waitcnt lgkmcnt(7)
	v_lshlrev_b32_e32 v66, 2, v66
	ds_write_b32 v66, v19
	s_and_b64 exec, s[2:3], s[8:9]
	s_waitcnt lgkmcnt(7)
	v_lshlrev_b32_e32 v67, 2, v67
	ds_write_b32 v67, v20
	s_and_b64 exec, s[2:3], s[10:11]
	s_waitcnt lgkmcnt(7)
	v_lshlrev_b32_e32 v68, 2, v68
	ds_write_b32 v68, v21
	s_and_b64 exec, s[2:3], s[12:13]
	s_waitcnt lgkmcnt(7)
	v_lshlrev_b32_e32 v69, 2, v69
	ds_write_b32 v69, v22
	s_and_b64 exec, s[2:3], s[14:15]
	s_waitcnt lgkmcnt(7)
	v_lshlrev_b32_e32 v70, 2, v70
	ds_write_b32 v70, v23
	s_and_b64 exec, s[2:3], s[16:17]
	s_waitcnt lgkmcnt(7)
	v_lshlrev_b32_e32 v71, 2, v71
	ds_write_b32 v71, v24
	s_and_b64 exec, s[2:3], s[18:19]
	s_waitcnt lgkmcnt(7)
	v_lshlrev_b32_e32 v72, 2, v72
	ds_write_b32 v72, v25
	s_and_b64 exec, s[2:3], s[22:23]
	s_waitcnt lgkmcnt(7)
	v_lshlrev_b32_e32 v73, 2, v73
	ds_write_b32 v73, v26
	s_waitcnt lgkmcnt(6)
	s_and_b64 exec, s[2:3], s[24:25]
	v_lshrrev_b32_e32 v82, 15, v27
	v_and_b32_e32 v82, 0x1fffc, v82
	v_add_u32_e32 v82, v18, v82
	ds_add_rtn_u32 v74, v82, v3
	s_and_b64 exec, s[2:3], s[26:27]
	v_lshrrev_b32_e32 v82, 15, v28
	v_and_b32_e32 v82, 0x1fffc, v82
	v_add_u32_e32 v82, v18, v82
	ds_add_rtn_u32 v75, v82, v3
	s_and_b64 exec, s[2:3], s[28:29]
	v_lshrrev_b32_e32 v82, 15, v29
	v_and_b32_e32 v82, 0x1fffc, v82
	v_add_u32_e32 v82, v18, v82
	ds_add_rtn_u32 v76, v82, v3
	s_and_b64 exec, s[2:3], s[30:31]
	v_lshrrev_b32_e32 v82, 15, v30
	v_and_b32_e32 v82, 0x1fffc, v82
	v_add_u32_e32 v82, v18, v82
	ds_add_rtn_u32 v77, v82, v3
	s_and_b64 exec, s[2:3], s[34:35]
	v_lshrrev_b32_e32 v82, 15, v31
	v_and_b32_e32 v82, 0x1fffc, v82
	v_add_u32_e32 v82, v18, v82
	ds_add_rtn_u32 v78, v82, v3
	s_and_b64 exec, s[2:3], s[36:37]
	v_lshrrev_b32_e32 v82, 15, v32
	v_and_b32_e32 v82, 0x1fffc, v82
	v_add_u32_e32 v82, v18, v82
	ds_add_rtn_u32 v79, v82, v3
	s_and_b64 exec, s[2:3], s[38:39]
	v_lshrrev_b32_e32 v82, 15, v33
	v_and_b32_e32 v82, 0x1fffc, v82
	v_add_u32_e32 v82, v18, v82
	ds_add_rtn_u32 v80, v82, v3
	s_and_b64 exec, s[2:3], s[40:41]
	v_lshrrev_b32_e32 v82, 15, v34
	v_and_b32_e32 v82, 0x1fffc, v82
	v_add_u32_e32 v82, v18, v82
	ds_add_rtn_u32 v81, v82, v3
	s_and_b64 exec, s[2:3], s[24:25]
	s_waitcnt lgkmcnt(7)
	v_lshlrev_b32_e32 v74, 2, v74
	ds_write_b32 v74, v27
	s_and_b64 exec, s[2:3], s[26:27]
	s_waitcnt lgkmcnt(7)
	v_lshlrev_b32_e32 v75, 2, v75
	ds_write_b32 v75, v28
	s_and_b64 exec, s[2:3], s[28:29]
	s_waitcnt lgkmcnt(7)
	v_lshlrev_b32_e32 v76, 2, v76
	ds_write_b32 v76, v29
	s_and_b64 exec, s[2:3], s[30:31]
	s_waitcnt lgkmcnt(7)
	v_lshlrev_b32_e32 v77, 2, v77
	ds_write_b32 v77, v30
	s_and_b64 exec, s[2:3], s[34:35]
	s_waitcnt lgkmcnt(7)
	v_lshlrev_b32_e32 v78, 2, v78
	ds_write_b32 v78, v31
	s_and_b64 exec, s[2:3], s[36:37]
	s_waitcnt lgkmcnt(7)
	v_lshlrev_b32_e32 v79, 2, v79
	ds_write_b32 v79, v32
	s_and_b64 exec, s[2:3], s[38:39]
	s_waitcnt lgkmcnt(7)
	v_lshlrev_b32_e32 v80, 2, v80
	ds_write_b32 v80, v33
	s_and_b64 exec, s[2:3], s[40:41]
	s_waitcnt lgkmcnt(7)
	v_lshlrev_b32_e32 v81, 2, v81
	ds_write_b32 v81, v34
	s_mov_b64 exec, s[2:3]
	s_and_b64 vcc, exec, s[42:43]
	s_cbranch_vccz .LBB2_251

amdhsa.kernels:
  - .agpr_count:     0
    .args:
      - .actual_access:  read_only
        .address_space:  global
        .offset:         0
        .size:           8
        .value_kind:     global_buffer
      - .actual_access:  read_only
        .address_space:  global
        .offset:         8
        .size:           8
        .value_kind:     global_buffer
      - .actual_access:  write_only
        .address_space:  global
        .offset:         16
        .size:           8
        .value_kind:     global_buffer
      - .actual_access:  write_only
        .address_space:  global
        .offset:         24
        .size:           8
        .value_kind:     global_buffer
      - .actual_access:  write_only
        .address_space:  global
        .offset:         32
        .size:           8
        .value_kind:     global_buffer
      - .actual_access:  write_only
        .address_space:  global
        .offset:         40
        .size:           8
        .value_kind:     global_buffer
      - .actual_access:  write_only
        .address_space:  global
        .offset:         48
        .size:           8
        .value_kind:     global_buffer
    .group_segment_fixed_size: 107840
    .kernarg_segment_align: 8
    .kernarg_segment_size: 56
    .language:       OpenCL C
    .language_version:
      - 2
      - 0
    .max_flat_workgroup_size: 1024
    .name:           _Z6k_partPKiS0_PjPtS1_S1_S1_
    .private_segment_fixed_size: 0
    .sgpr_count:     50
    .sgpr_spill_count: 0
    .symbol:         _Z6k_partPKiS0_PjPtS1_S1_S1_.kd
    .uniform_work_group_size: 1
    .uses_dynamic_stack: false
    .vgpr_count:     123
    .vgpr_spill_count: 0
    .wavefront_size: 64
  - .agpr_count:     0
    .args:
      - .actual_access:  read_only
        .address_space:  global
        .offset:         0
        .size:           8
        .value_kind:     global_buffer
      - .actual_access:  read_only
        .address_space:  global
        .offset:         8
        .size:           8
        .value_kind:     global_buffer
      - .actual_access:  read_only
        .address_space:  global
        .offset:         16
        .size:           8
        .value_kind:     global_buffer
      - .actual_access:  read_only
        .address_space:  global
        .offset:         24
        .size:           8
        .value_kind:     global_buffer
      - .actual_access:  write_only
        .address_space:  global
        .offset:         32
        .size:           8
        .value_kind:     global_buffer
      - .actual_access:  write_only
        .address_space:  global
        .offset:         40
        .size:           8
        .value_kind:     global_buffer
    .group_segment_fixed_size: 103492
    .kernarg_segment_align: 8
    .kernarg_segment_size: 48
    .language:       OpenCL C
    .language_version:
      - 2
      - 0
    .max_flat_workgroup_size: 320
    .name:           _Z6k_gemmPKfS0_PKtPKjPfPt
    .private_segment_fixed_size: 0
    .sgpr_count:     43
    .sgpr_spill_count: 0
    .symbol:         _Z6k_gemmPKfS0_PKtPKjPfPt.kd
    .uniform_work_group_size: 1
    .uses_dynamic_stack: false
    .vgpr_count:     192
    .vgpr_spill_count: 0
    .wavefront_size: 64
  - .agpr_count:     0
    .args:
      - .actual_access:  read_only
        .address_space:  global
        .offset:         0
        .size:           8
        .value_kind:     global_buffer
      - .actual_access:  read_only
        .address_space:  global
        .offset:         8
        .size:           8
        .value_kind:     global_buffer
      - .actual_access:  read_only
        .address_space:  global
        .offset:         16
        .size:           8
        .value_kind:     global_buffer
      - .actual_access:  read_only
        .address_space:  global
        .offset:         24
        .size:           8
        .value_kind:     global_buffer
      - .actual_access:  read_only
        .address_space:  global
        .offset:         32
        .size:           8
        .value_kind:     global_buffer
      - .address_space:  global
        .offset:         40
        .size:           8
        .value_kind:     global_buffer
      - .actual_access:  read_only
        .address_space:  global
        .offset:         48
        .size:           8
        .value_kind:     global_buffer
      - .actual_access:  read_only
        .address_space:  global
        .offset:         56
        .size:           8
        .value_kind:     global_buffer
      - .actual_access:  write_only
        .address_space:  global
        .offset:         64
        .size:           8
        .value_kind:     global_buffer
      - .address_space:  global
        .offset:         72
        .size:           8
        .value_kind:     global_buffer
      - .offset:         80
        .size:           4
        .value_kind:     hidden_block_count_x
      - .offset:         84
        .size:           4
        .value_kind:     hidden_block_count_y
      - .offset:         88
        .size:           4
        .value_kind:     hidden_block_count_z
      - .offset:         92
        .size:           2
        .value_kind:     hidden_group_size_x
      - .offset:         94
        .size:           2
        .value_kind:     hidden_group_size_y
      - .offset:         96
        .size:           2
        .value_kind:     hidden_group_size_z
      - .offset:         98
        .size:           2
        .value_kind:     hidden_remainder_x
      - .offset:         100
        .size:           2
        .value_kind:     hidden_remainder_y
      - .offset:         102
        .size:           2
        .value_kind:     hidden_remainder_z
      - .offset:         120
        .size:           8
        .value_kind:     hidden_global_offset_x
      - .offset:         128
        .size:           8
        .value_kind:     hidden_global_offset_y
      - .offset:         136
        .size:           8
        .value_kind:     hidden_global_offset_z
      - .offset:         144
        .size:           2
        .value_kind:     hidden_grid_dims
    .group_segment_fixed_size: 97600
    .kernarg_segment_align: 8
    .kernarg_segment_size: 336
    .language:       OpenCL C
    .language_version:
      - 2
      - 0
    .max_flat_workgroup_size: 1024
    .name:           _Z6k_aggfPKjS0_PKtPKfS4_PtS4_S4_PfPj
    .private_segment_fixed_size: 0
    .sgpr_count:     81
    .sgpr_spill_count: 0
    .symbol:         _Z6k_aggfPKjS0_PKtPKfS4_PtS4_S4_PfPj.kd
    .uniform_work_group_size: 1
    .uses_dynamic_stack: false
    .vgpr_count:     128
    .vgpr_spill_count: 0
    .wavefront_size: 64
